# prologue: exec-masked diagonal-select ladders replaced by straight-line v_cndmask selects
# speedup vs baseline: 1.0347x; 1.0080x over previous
.Lno_stagger:
	v_cvt_pk_f16_f32 v2, -v2, -v3
	v_cvt_pk_f16_f32 v3, -v4, -v5
	v_mad_u32_u24 v4, v42, s5, v93
	ds_write_b64 v4, v[2:3]
	s_waitcnt vmcnt(14)
	v_cvt_pk_f16_f32 v2, -v6, -v7
	v_cvt_pk_f16_f32 v3, -v8, -v9
	v_mad_u32_u24 v4, v43, s5, v93
	ds_write_b64 v4, v[2:3]
	s_waitcnt vmcnt(13)
	v_cvt_pk_f16_f32 v2, -v10, -v11
	v_cvt_pk_f16_f32 v3, -v12, -v13
	v_mad_u32_u24 v4, v44, s5, v93
	ds_write_b64 v4, v[2:3]
	s_waitcnt vmcnt(12)
	v_cvt_pk_f16_f32 v2, -v14, -v15
	v_cvt_pk_f16_f32 v3, -v16, -v17
	v_mad_u32_u24 v4, v45, s5, v93
	ds_write_b64 v4, v[2:3]
	s_waitcnt vmcnt(11)
	v_cvt_pk_f16_f32 v2, -v46, -v47
	v_cvt_pk_f16_f32 v3, -v48, -v49
	v_bitop3_b32 v46, s25, v70, 16 bitop3:0xde
	v_mad_u32_u24 v4, v46, s5, v93
	ds_write_b64 v4, v[2:3]
	s_waitcnt vmcnt(10)
	v_cvt_pk_f16_f32 v2, -v50, -v51
	v_cvt_pk_f16_f32 v3, -v52, -v53
	v_or_b32_e32 v47, s38, v70
	v_mad_u32_u24 v4, v47, s5, v93
	ds_write_b64 v4, v[2:3]
	s_waitcnt vmcnt(9)
	v_cvt_pk_f16_f32 v2, -v58, -v59
	v_cvt_pk_f16_f32 v3, -v60, -v61
	v_or_b32_e32 v48, s39, v70
	v_mad_u32_u24 v4, v48, s5, v93
	ds_write_b64 v4, v[2:3]
	s_waitcnt vmcnt(8)
	v_cvt_pk_f16_f32 v2, -v62, -v63
	v_cvt_pk_f16_f32 v3, -v64, -v65
	v_or_b32_e32 v49, s40, v70
	v_mad_u32_u24 v4, v49, s5, v93
	ds_write_b64 v4, v[2:3]
	s_waitcnt lgkmcnt(0)
	ds_read_b128 v[98:101], v82
	ds_read_b128 v[102:105], v82 offset:32
	s_waitcnt lgkmcnt(1)
	v_mfma_f32_32x32x16_f16 v[2:17], v[98:101], v[98:101], 0
	ds_read_b128 v[106:109], v82 offset:64
	ds_read_b128 v[110:113], v82 offset:96
	s_waitcnt lgkmcnt(0)
	v_and_b32_e32 v50, 3, v0
	v_cmp_ne_u32_e64 s[6:7], 0, v50
	v_cmp_ne_u32_e64 s[4:5], 1, v50
	v_cmp_eq_u32_e32 vcc, 2, v50
	s_waitcnt lgkmcnt(2)
	v_mfma_f32_32x32x16_f16 v[2:17], v[102:105], v[102:105], v[2:17]
	s_waitcnt lgkmcnt(1)
	v_mfma_f32_32x32x16_f16 v[2:17], v[106:109], v[106:109], v[2:17]
	s_waitcnt lgkmcnt(0)
	v_mfma_f32_32x32x16_f16 v[2:17], v[110:113], v[110:113], v[2:17]
	s_nop 11
	v_cndmask_b32_e32 v5, v5, v4, vcc
	v_cndmask_b32_e32 v9, v9, v8, vcc
	v_cndmask_b32_e32 v13, v13, v12, vcc
	v_cndmask_b32_e32 v17, v17, v16, vcc
	v_cndmask_b32_e64 v3, v3, v5, s[4:5]
	v_cndmask_b32_e64 v7, v7, v9, s[4:5]
	v_cndmask_b32_e64 v11, v11, v13, s[4:5]
	v_cndmask_b32_e64 v15, v15, v17, s[4:5]
	v_cndmask_b32_e64 v2, v2, v3, s[6:7]
	v_cndmask_b32_e64 v6, v6, v7, s[6:7]
	v_cndmask_b32_e64 v10, v10, v11, s[6:7]
	v_cndmask_b32_e64 v14, v14, v15, s[6:7]
	v_mov_b32_e32 v13, 0x1e400
	v_lshl_or_b32 v13, v181, 2, v13
	v_lshrrev_b32_e32 v15, 3, v181
	v_bfe_u32 v16, v0, 2, 1
	v_mul_u32_u24_e32 v12, 0x90, v42
	v_mul_u32_u24_e32 v11, 0x90, v43
	v_mul_u32_u24_e32 v9, 0x90, v44
	v_mul_u32_u24_e32 v8, 0x90, v45
	v_mul_u32_u24_e32 v7, 0x90, v46
	v_mul_u32_u24_e32 v5, 0x90, v47
	v_mul_u32_u24_e32 v4, 0x90, v48
	v_mul_u32_u24_e32 v3, 0x90, v49
	v_cmp_eq_u32_e64 s[16:17], v184, v16
	v_cmp_gt_u32_e64 s[8:9], 8, v181
	v_cmp_eq_u32_e64 s[12:13], 1, v15
	v_cmp_eq_u32_e64 s[14:15], 2, v15
	v_lshl_add_u32 v83, s3, 2, v13
	s_and_saveexec_b64 s[28:29], s[16:17]
	v_cndmask_b32_e64 v10, v14, v10, s[14:15]
	v_cndmask_b32_e64 v6, v10, v6, s[12:13]
	v_cndmask_b32_e64 v2, v6, v2, s[8:9]
	v_mul_f32_e32 v2, 0.5, v2
	ds_write_b32 v83, v2
	s_or_b64 exec, exec, s[28:29]
	v_add3_u32 v2, v85, s3, 32
	v_or_b32_e32 v6, s25, v2
	v_lshl_or_b32 v6, v6, 8, v84
	v_or_b32_e32 v10, s34, v2
	v_lshl_or_b32 v10, v10, 8, v84
	global_load_dwordx4 v[78:81], v6, s[22:23]
	global_load_dwordx4 v[70:73], v10, s[22:23]
	v_or_b32_e32 v6, s35, v2
	v_lshl_or_b32 v6, v6, 8, v84
	v_or_b32_e32 v10, s36, v2
	v_lshl_or_b32 v10, v10, 8, v84
	global_load_dwordx4 v[74:77], v6, s[22:23]
	global_load_dwordx4 v[58:61], v10, s[22:23]
	v_or_b32_e32 v6, s37, v2
	v_lshl_or_b32 v6, v6, 8, v84
	v_or_b32_e32 v10, s38, v2
	v_lshl_or_b32 v10, v10, 8, v84
	global_load_dwordx4 v[62:65], v6, s[22:23]
	global_load_dwordx4 v[46:49], v10, s[22:23]
	v_or_b32_e32 v6, s39, v2
	v_lshl_or_b32 v6, v6, 8, v84
	v_or_b32_e32 v2, s40, v2
	v_lshl_or_b32 v2, v2, 8, v84
	global_load_dwordx4 v[50:53], v6, s[22:23]
	global_load_dwordx4 v[42:45], v2, s[22:23]
	s_waitcnt vmcnt(15)
	v_cvt_pk_f16_f32 v14, -v66, -v67
	v_cvt_pk_f16_f32 v15, -v68, -v69
	v_add_u32_e32 v86, v93, v12
	ds_write_b64 v86, v[14:15]
	s_waitcnt vmcnt(14)
	v_cvt_pk_f16_f32 v12, -v54, -v55
	v_cvt_pk_f16_f32 v13, -v56, -v57
	v_add_u32_e32 v87, v93, v11
	ds_write_b64 v87, v[12:13]
	s_waitcnt vmcnt(13)
	v_cvt_pk_f16_f32 v10, -v38, -v39
	v_cvt_pk_f16_f32 v11, -v40, -v41
	v_add_u32_e32 v88, v93, v9
	ds_write_b64 v88, v[10:11]
	s_waitcnt vmcnt(12)
	v_cvt_pk_f16_f32 v10, -v34, -v35
	v_cvt_pk_f16_f32 v11, -v36, -v37
	v_add_u32_e32 v89, v93, v8
	ds_write_b64 v89, v[10:11]
	s_waitcnt vmcnt(11)
	v_cvt_pk_f16_f32 v8, -v30, -v31
	v_cvt_pk_f16_f32 v9, -v32, -v33
	v_add_u32_e32 v90, v93, v7
	ds_write_b64 v90, v[8:9]
	s_waitcnt vmcnt(10)
	v_cvt_pk_f16_f32 v6, -v26, -v27
	v_cvt_pk_f16_f32 v7, -v28, -v29
	v_add_u32_e32 v91, v93, v5
	ds_write_b64 v91, v[6:7]
	s_waitcnt vmcnt(9)
	v_cvt_pk_f16_f32 v6, -v22, -v23
	v_cvt_pk_f16_f32 v7, -v24, -v25
	v_add_u32_e32 v92, v93, v4
	ds_write_b64 v92, v[6:7]
	s_waitcnt vmcnt(8)
	v_cvt_pk_f16_f32 v4, -v18, -v19
	v_cvt_pk_f16_f32 v5, -v20, -v21
	v_add_u32_e32 v93, v93, v3
	ds_write_b64 v93, v[4:5]
	s_waitcnt lgkmcnt(0)
	ds_read_b128 v[114:117], v82
	ds_read_b128 v[118:121], v82 offset:32
	s_waitcnt lgkmcnt(1)
	v_mfma_f32_32x32x16_f16 v[2:17], v[114:117], v[114:117], 0
	ds_read_b128 v[122:125], v82 offset:64
	ds_read_b128 v[126:129], v82 offset:96
	s_waitcnt lgkmcnt(0)
	s_waitcnt lgkmcnt(2)
	v_mfma_f32_32x32x16_f16 v[2:17], v[118:121], v[118:121], v[2:17]
	s_waitcnt lgkmcnt(1)
	v_mfma_f32_32x32x16_f16 v[2:17], v[122:125], v[122:125], v[2:17]
	s_waitcnt lgkmcnt(0)
	v_mfma_f32_32x32x16_f16 v[2:17], v[126:129], v[126:129], v[2:17]
	s_nop 11
	v_cndmask_b32_e32 v5, v5, v4, vcc
	v_cndmask_b32_e32 v9, v9, v8, vcc
	v_cndmask_b32_e32 v13, v13, v12, vcc
	v_cndmask_b32_e32 v17, v17, v16, vcc
	v_cndmask_b32_e64 v3, v3, v5, s[4:5]
	v_cndmask_b32_e64 v7, v7, v9, s[4:5]
	v_cndmask_b32_e64 v11, v11, v13, s[4:5]
	v_cndmask_b32_e64 v15, v15, v17, s[4:5]
	v_cndmask_b32_e64 v2, v2, v3, s[6:7]
	v_cndmask_b32_e64 v6, v6, v7, s[6:7]
	v_cndmask_b32_e64 v10, v10, v11, s[6:7]
	v_cndmask_b32_e64 v14, v14, v15, s[6:7]
	s_and_saveexec_b64 s[28:29], s[16:17]
	v_cndmask_b32_e64 v3, v14, v10, s[14:15]
	v_cndmask_b32_e64 v3, v3, v6, s[12:13]
	v_cndmask_b32_e64 v2, v3, v2, s[8:9]
	v_mul_f32_e32 v2, 0.5, v2
	ds_write_b32 v83, v2 offset:128
	s_or_b64 exec, exec, s[28:29]
	v_add3_u32 v2, v85, s3, 64
	v_or_b32_e32 v3, s25, v2
	v_lshl_or_b32 v3, v3, 8, v84
	v_or_b32_e32 v4, s34, v2
	v_lshl_or_b32 v4, v4, 8, v84
	global_load_dwordx4 v[66:69], v3, s[22:23]
	global_load_dwordx4 v[38:41], v4, s[22:23]
	v_or_b32_e32 v3, s35, v2
	v_lshl_or_b32 v3, v3, 8, v84
	v_or_b32_e32 v4, s36, v2
	v_lshl_or_b32 v4, v4, 8, v84
	global_load_dwordx4 v[54:57], v3, s[22:23]
	global_load_dwordx4 v[30:33], v4, s[22:23]
	v_or_b32_e32 v3, s37, v2
	v_lshl_or_b32 v3, v3, 8, v84
	v_or_b32_e32 v4, s38, v2
	v_lshl_or_b32 v4, v4, 8, v84
	global_load_dwordx4 v[34:37], v3, s[22:23]
	global_load_dwordx4 v[22:25], v4, s[22:23]
	v_or_b32_e32 v3, s39, v2
	v_lshl_or_b32 v3, v3, 8, v84
	v_or_b32_e32 v2, s40, v2
	v_lshl_or_b32 v2, v2, 8, v84
	global_load_dwordx4 v[26:29], v3, s[22:23]
	global_load_dwordx4 v[18:21], v2, s[22:23]
	s_waitcnt vmcnt(15)
	v_cvt_pk_f16_f32 v2, -v78, -v79
	v_cvt_pk_f16_f32 v3, -v80, -v81
	ds_write_b64 v86, v[2:3]
	s_waitcnt vmcnt(14)
	v_cvt_pk_f16_f32 v2, -v70, -v71
	v_cvt_pk_f16_f32 v3, -v72, -v73
	ds_write_b64 v87, v[2:3]
	s_waitcnt vmcnt(13)
	v_cvt_pk_f16_f32 v2, -v74, -v75
	v_cvt_pk_f16_f32 v3, -v76, -v77
	ds_write_b64 v88, v[2:3]
	s_waitcnt vmcnt(12)
	v_cvt_pk_f16_f32 v2, -v58, -v59
	v_cvt_pk_f16_f32 v3, -v60, -v61
	ds_write_b64 v89, v[2:3]
	s_waitcnt vmcnt(11)
	v_cvt_pk_f16_f32 v2, -v62, -v63
	v_cvt_pk_f16_f32 v3, -v64, -v65
	ds_write_b64 v90, v[2:3]
	s_waitcnt vmcnt(10)
	v_cvt_pk_f16_f32 v2, -v46, -v47
	v_cvt_pk_f16_f32 v3, -v48, -v49
	ds_write_b64 v91, v[2:3]
	s_waitcnt vmcnt(9)
	v_cvt_pk_f16_f32 v2, -v50, -v51
	v_cvt_pk_f16_f32 v3, -v52, -v53
	ds_write_b64 v92, v[2:3]
	s_waitcnt vmcnt(8)
	v_cvt_pk_f16_f32 v2, -v42, -v43
	v_cvt_pk_f16_f32 v3, -v44, -v45
	ds_write_b64 v93, v[2:3]
	s_waitcnt lgkmcnt(0)
	ds_read_b128 v[130:133], v82
	ds_read_b128 v[134:137], v82 offset:32
	s_waitcnt lgkmcnt(1)
	v_mfma_f32_32x32x16_f16 v[2:17], v[130:133], v[130:133], 0
	ds_read_b128 v[138:141], v82 offset:64
	ds_read_b128 v[142:145], v82 offset:96
	s_waitcnt lgkmcnt(0)
	s_waitcnt lgkmcnt(2)
	v_mfma_f32_32x32x16_f16 v[2:17], v[134:137], v[134:137], v[2:17]
	s_waitcnt lgkmcnt(1)
	v_mfma_f32_32x32x16_f16 v[2:17], v[138:141], v[138:141], v[2:17]
	s_waitcnt lgkmcnt(0)
	v_mfma_f32_32x32x16_f16 v[2:17], v[142:145], v[142:145], v[2:17]
	s_nop 11
	v_cndmask_b32_e32 v5, v5, v4, vcc
	v_cndmask_b32_e32 v9, v9, v8, vcc
	v_cndmask_b32_e32 v13, v13, v12, vcc
	v_cndmask_b32_e32 v17, v17, v16, vcc
	v_cndmask_b32_e64 v3, v3, v5, s[4:5]
	v_cndmask_b32_e64 v7, v7, v9, s[4:5]
	v_cndmask_b32_e64 v11, v11, v13, s[4:5]
	v_cndmask_b32_e64 v15, v15, v17, s[4:5]
	v_cndmask_b32_e64 v2, v2, v3, s[6:7]
	v_cndmask_b32_e64 v6, v6, v7, s[6:7]
	v_cndmask_b32_e64 v10, v10, v11, s[6:7]
	v_cndmask_b32_e64 v14, v14, v15, s[6:7]
	s_and_saveexec_b64 s[28:29], s[16:17]
	v_cndmask_b32_e64 v3, v14, v10, s[14:15]
	v_cndmask_b32_e64 v3, v3, v6, s[12:13]
	v_cndmask_b32_e64 v2, v3, v2, s[8:9]
	v_mul_f32_e32 v2, 0.5, v2
	ds_write_b32 v83, v2 offset:256
	s_or_b64 exec, exec, s[28:29]
	s_waitcnt vmcnt(7)
	v_cvt_pk_f16_f32 v2, -v66, -v67
	v_cvt_pk_f16_f32 v3, -v68, -v69
	ds_write_b64 v86, v[2:3]
	s_waitcnt vmcnt(6)
	v_cvt_pk_f16_f32 v2, -v38, -v39
	v_cvt_pk_f16_f32 v3, -v40, -v41
	ds_write_b64 v87, v[2:3]
	s_waitcnt vmcnt(5)
	v_cvt_pk_f16_f32 v2, -v54, -v55
	v_cvt_pk_f16_f32 v3, -v56, -v57
	ds_write_b64 v88, v[2:3]
	s_waitcnt vmcnt(4)
	v_cvt_pk_f16_f32 v2, -v30, -v31
	v_cvt_pk_f16_f32 v3, -v32, -v33
	ds_write_b64 v89, v[2:3]
	s_waitcnt vmcnt(3)
	v_cvt_pk_f16_f32 v2, -v34, -v35
	v_cvt_pk_f16_f32 v3, -v36, -v37
	ds_write_b64 v90, v[2:3]
	s_waitcnt vmcnt(2)
	v_cvt_pk_f16_f32 v2, -v22, -v23
	v_cvt_pk_f16_f32 v3, -v24, -v25
	ds_write_b64 v91, v[2:3]
	s_waitcnt vmcnt(1)
	v_cvt_pk_f16_f32 v2, -v26, -v27
	v_cvt_pk_f16_f32 v3, -v28, -v29
	ds_write_b64 v92, v[2:3]
	s_waitcnt vmcnt(0)
	v_cvt_pk_f16_f32 v2, -v18, -v19
	v_cvt_pk_f16_f32 v3, -v20, -v21
	ds_write_b64 v93, v[2:3]
	s_waitcnt lgkmcnt(0)
	ds_read_b128 v[146:149], v82
	ds_read_b128 v[150:153], v82 offset:32
	s_waitcnt lgkmcnt(1)
	v_mfma_f32_32x32x16_f16 v[2:17], v[146:149], v[146:149], 0
	ds_read_b128 v[154:157], v82 offset:64
	ds_read_b128 v[158:161], v82 offset:96
	s_waitcnt lgkmcnt(0)
	s_waitcnt lgkmcnt(2)
	v_mfma_f32_32x32x16_f16 v[2:17], v[150:153], v[150:153], v[2:17]
	s_waitcnt lgkmcnt(1)
	v_mfma_f32_32x32x16_f16 v[2:17], v[154:157], v[154:157], v[2:17]
	s_waitcnt lgkmcnt(0)
	v_mfma_f32_32x32x16_f16 v[2:17], v[158:161], v[158:161], v[2:17]
	s_nop 11
	v_cndmask_b32_e32 v5, v5, v4, vcc
	v_cndmask_b32_e32 v9, v9, v8, vcc
	v_cndmask_b32_e32 v13, v13, v12, vcc
	v_cndmask_b32_e32 v17, v17, v16, vcc
	v_cndmask_b32_e64 v3, v3, v5, s[4:5]
	v_cndmask_b32_e64 v7, v7, v9, s[4:5]
	v_cndmask_b32_e64 v11, v11, v13, s[4:5]
	v_cndmask_b32_e64 v15, v15, v17, s[4:5]
	v_cndmask_b32_e64 v2, v2, v3, s[6:7]
	v_cndmask_b32_e64 v6, v6, v7, s[6:7]
	v_cndmask_b32_e64 v10, v10, v11, s[6:7]
	v_cndmask_b32_e64 v14, v14, v15, s[6:7]
	s_and_saveexec_b64 s[4:5], s[16:17]
	v_cndmask_b32_e64 v3, v14, v10, s[14:15]
	v_cndmask_b32_e64 v3, v3, v6, s[12:13]
	v_cndmask_b32_e64 v2, v3, v2, s[8:9]
	v_mul_f32_e32 v2, 0.5, v2
	ds_write_b32 v83, v2 offset:384
	s_or_b64 exec, exec, s[4:5]
	v_lshl_or_b32 v2, s33, 9, v182
	s_waitcnt lgkmcnt(0)
	v_add_u32_e32 v62, 0x1e400, v2
	ds_read_b128 v[2:5], v62
	ds_read_b128 v[6:9], v62 offset:32
	ds_read_b128 v[10:13], v62 offset:64
	ds_read_b128 v[14:17], v62 offset:96
	ds_read_b128 v[18:21], v62 offset:128
	ds_read_b128 v[22:25], v62 offset:160
	ds_read_b128 v[26:29], v62 offset:192
	ds_read_b128 v[30:33], v62 offset:224
	ds_read_b128 v[34:37], v62 offset:256
	ds_read_b128 v[38:41], v62 offset:288
	ds_read_b128 v[42:45], v62 offset:320
	ds_read_b128 v[46:49], v62 offset:352
	ds_read_b128 v[50:53], v62 offset:384
	ds_read_b128 v[54:57], v62 offset:416
	ds_read_b128 v[58:61], v62 offset:448
	ds_read_b128 v[62:65], v62 offset:480
	v_cndmask_b32_e64 v66, 0, 1, s[26:27]
	v_mul_u32_u24_e32 v185, 0x90, v181
	v_cmp_ne_u32_e64 s[4:5], 1, v66
	s_andn2_b64 vcc, exec, s[26:27]
	v_lshlrev_b32_e32 v66, 3, v1
	v_lshlrev_b32_e32 v186, 8, v183
	s_waitcnt lgkmcnt(0)
	s_barrier
	s_cbranch_vccnz .LBB0_79
	v_and_b32_e32 v67, 0xff, v0
	v_mov_b32_e32 v72, 0x12000
	v_lshl_or_b32 v67, v67, 4, v72
	s_mov_b32 s6, 0x13000
	ds_write_b128 v67, v[174:177]
	v_or3_b32 v67, v186, v178, s6
	ds_write_b128 v67, v[170:173]
	v_or_b32_e32 v67, s24, v183
	v_or_b32_e32 v72, 64, v67
	v_ashrrev_i32_e32 v73, 31, v72
	v_or_b32_e32 v74, 0x50, v67
	v_lshlrev_b64 v[72:73], 8, v[72:73]
	v_ashrrev_i32_e32 v75, 31, v74
	v_lshl_add_u64 v[72:73], s[20:21], 0, v[72:73]
	v_mov_b32_e32 v179, 0
	v_lshlrev_b64 v[74:75], 8, v[74:75]
	v_lshl_add_u64 v[72:73], v[72:73], 0, v[178:179]
	v_lshl_add_u64 v[74:75], s[20:21], 0, v[74:75]
	v_cvt_pk_f16_f32 v69, v176, v177
	v_cvt_pk_f16_f32 v68, v174, v175
	v_cvt_pk_f16_f32 v71, v172, v173
	v_cvt_pk_f16_f32 v70, v170, v171
	v_lshl_add_u64 v[74:75], v[74:75], 0, v[178:179]
	global_load_dwordx4 v[174:177], v[72:73], off nt
	global_load_dwordx4 v[170:173], v[74:75], off nt
	s_movk_i32 s6, 0x90
	v_mad_u32_u24 v67, v183, s6, v66
	ds_write_b64 v67, v[68:69]
	ds_write_b64 v67, v[70:71] offset:2304
